# barrier-wait conversion with four waves x 16-row half slabs (same bytes per barrier, shorter per-wave latency chain) instead of two waves x 32 rows
# baseline (speedup 1.0000x reference)
; #define LAS __attribute__((address_space(3)))
; #define SB() __builtin_amdgcn_sched_barrier(0)
; #define LDS_WAIT() asm volatile("s_waitcnt lgkmcnt(0)" ::: "memory")
; __device__ __forceinline__ unsigned cvt_pk_bf16(float lo, float hi) { unsigned r; asm volatile("v_cvt_pk_bf16_f32 %0, %1, %2" : "=v"(r) : "v"(lo), "v"(hi)); return r; }
; __device__ __forceinline__ int lane_id_v() { int l; asm volatile("v_mbcnt_lo_u32_b32 %0, -1, 0\n\tv_mbcnt_hi_u32_b32 %0, -1, %0" : "=v"(l)); return l; }
; __device__ __forceinline__ void wg_convert_tile(Frame& F, const float* W, int ldw, bf16_t* WT, int Kd, int k0, int n0, int kind, const float* kgain) {
;     const int lane = lane_id_v(), w = F.wave;
;     LAS unsigned char* img = F.lds;
;     const float* src = W + (size_t)(k0 + 8 * w) * ldw + n0 + 4 * lane;
;     f32x4 ld[2][8];
; #pragma unroll
;     for (int j = 0; j < 8; ++j) ld[0][j] = __builtin_nontemporal_load((const f32x4*)(src + (size_t)j * ldw));
; #pragma unroll
;     for (int p = 0; p < 4; ++p) {
;         if (p < 3) {
; #pragma unroll
;             for (int j = 0; j < 8; ++j) ld[(p + 1) & 1][j] = __builtin_nontemporal_load((const f32x4*)(src + (size_t)(64 * (p + 1) + j) * ldw)); }
;         float g[8];
; #pragma unroll
;         for (int j = 0; j < 8; ++j) g[j] = kgain ? kgain[k0 + 64 * p + 8 * w + j] : 1.f;
;         SB();
;         const unsigned kc = (unsigned)(8 * p + w);
; #pragma unroll
;         for (int c = 0; c < 4; ++c) { const int n = 4 * lane + c;
;             u32x4 o; o.x = cvt_pk_bf16(ld[p & 1][0][c] * g[0], ld[p & 1][1][c] * g[1]); o.y = cvt_pk_bf16(ld[p & 1][2][c] * g[2], ld[p & 1][3][c] * g[3]);
;                      o.z = cvt_pk_bf16(ld[p & 1][4][c] * g[4], ld[p & 1][5][c] * g[5]); o.w = cvt_pk_bf16(ld[p & 1][6][c] * g[6], ld[p & 1][7][c] * g[7]);
;             *(LAS u32x4*)(img + n * 512 + ((kc ^ (unsigned)(lane & 31)) << 4)) = o; }
;         SB();
;     }
;     LDS_WAIT(); __syncthreads();
.Lbw_run:
	v_writelane_b32 v253, s6, 40
	v_writelane_b32 v253, s7, 41
	v_writelane_b32 v253, s8, 42
	v_writelane_b32 v253, s9, 43
	v_writelane_b32 v253, s10, 44
	v_writelane_b32 v253, s11, 45
	v_writelane_b32 v253, s12, 46
	v_writelane_b32 v253, s13, 47
	v_writelane_b32 v253, s14, 48
	v_writelane_b32 v253, s15, 49
	v_writelane_b32 v253, s32, 50
	v_writelane_b32 v253, s33, 51
	v_writelane_b32 v253, s34, 52
	v_writelane_b32 v253, s35, 53
	v_writelane_b32 v253, s36, 54
	v_writelane_b32 v253, s37, 55
	v_writelane_b32 v253, s38, 56
	v_writelane_b32 v253, s39, 57
	v_readlane_b32 s6, v251, 2
	v_readlane_b32 s7, v253, 63
	v_readlane_b32 s9, v251, 3
	v_readlane_b32 s12, v251, 9
	v_readlane_b32 s13, v251, 10
	s_nop 4
	s_sub_u32 s6, s6, 1
	s_cmp_gt_u32 s6, 3
	s_cbranch_scc1 .Lbw_out
	s_cmp_ge_u32 s7, 16
	s_cbranch_scc1 .Lbw_out
	s_add_u32 s8, s7, 1
	s_nop 0
	v_writelane_b32 v253, s8, 63
	s_mov_b64 exec, -1
	s_load_dwordx2 s[14:15], s[12:13], 0xe0
	v_mbcnt_lo_u32_b32 v2, -1, 0
	v_mbcnt_hi_u32_b32 v2, -1, v2
	s_mul_i32 s7, s7, 4
	s_add_u32 s7, s7, s6
	s_lshr_b32 s8, s7, 4
	s_and_b32 s7, s7, 15
	s_lshr_b32 s9, s9, 3
	s_add_u32 s8, s8, 4
	s_lshl_b32 s8, s8, 8
	s_add_u32 s8, s8, s9
	s_sub_u32 s8, s8, 0x210
	s_mul_i32 s9, s8, 0xaaab
	s_lshr_b32 s9, s9, 21
	s_mul_i32 s10, s9, 48
	s_sub_u32 s8, s8, s10
	s_lshr_b32 s10, s8, 4
	s_and_b32 s8, s8, 15
	s_add_u32 s11, s9, 32
	s_lshl_b32 s11, s11, 22
	v_lshlrev_b32_e32 v3, 4, v2
	v_and_b32_e32 v10, 31, v2
	v_lshlrev_b32_e32 v10, 2, v10
	s_cmp_eq_u32 s10, 2
	s_cbranch_scc1 .Lbw_k2
	s_lshl_b32 s32, s10, 3
	s_addk_i32 s32, 0xc0
	s_load_dwordx2 s[34:35], s[12:13], s32 offset:0x0
	s_load_dwordx2 s[36:37], s[12:13], 0x98
	s_lshr_b32 s33, s8, 1
	s_and_b32 s8, s8, 1
	s_lshl_b32 s38, s33, 19
	s_add_u32 s11, s11, s38
	s_lshl_b32 s38, s8, 10
	s_add_u32 s11, s11, s38
	s_lshl_b32 s38, s7, 15
	s_add_u32 s11, s11, s38
	s_movk_i32 s32, 0x800
	s_lshl_b32 s38, s9, 22
	s_add_u32 s38, s38, 0x10500000
	s_lshl_b32 s39, s8, 21
	s_add_u32 s38, s38, s39
	s_lshl_b32 s39, s10, 19
	s_add_u32 s38, s38, s39
	s_lshl_b32 s39, s33, 9
	s_add_u32 s38, s38, s39
	s_lshl_b32 s39, s7, 5
	s_add_u32 s38, s38, s39
	s_lshl_b32 s39, s33, 10
	s_lshl_b32 s33, s7, 6
	s_add_u32 s39, s39, s33
	s_addk_i32 s39, 0x2000
	s_movk_i32 s33, 0x1000
	s_mov_b32 s10, 1
	s_waitcnt lgkmcnt(0)
	s_add_u32 s36, s36, s39
	s_addc_u32 s37, s37, 0
	global_load_dword v9, v10, s[36:37]
	s_branch .Lbw_go
.Lbw_k2:
	s_load_dwordx2 s[34:35], s[12:13], 0xd0
	s_lshr_b32 s33, s8, 3
	s_and_b32 s8, s8, 7
	s_lshl_b32 s38, s33, 21
	s_add_u32 s11, s11, s38
	s_lshl_b32 s38, s8, 10
	s_add_u32 s11, s11, s38
	s_lshl_b32 s38, s7, 17
	s_add_u32 s11, s11, s38
	s_movk_i32 s32, 0x2000
	s_lshl_b32 s38, s9, 21
	s_add_u32 s38, s38, 0x1c500000
	s_lshl_b32 s39, s8, 18
	s_add_u32 s38, s38, s39
	s_lshl_b32 s39, s33, 9
	s_add_u32 s38, s38, s39
	s_lshl_b32 s39, s7, 5
	s_add_u32 s38, s38, s39
	s_movk_i32 s33, 0x400
	s_mov_b32 s10, 0
	s_waitcnt lgkmcnt(0)
	global_load_dword v9, v10, s[34:35]
.Lbw_go:
	s_add_u32 s6, s6, 1
	s_lshl_b32 s6, s6, 14
	v_lshl_add_u32 v5, v2, 7, s6
	v_and_b32_e32 v6, 7, v2
	v_lshrrev_b32_e32 v7, 3, v2
	v_and_b32_e32 v18, 7, v7
	v_xor_b32_e32 v18, v18, v6
	v_lshl_add_u32 v17, v7, 7, s6
	v_lshl_add_u32 v17, v18, 4, v17
	v_lshrrev_b32_e32 v8, 1, v2
	v_mul_lo_u32 v8, v8, s33
	v_and_b32_e32 v11, 1, v2
	v_lshl_add_u32 v8, v11, 4, v8
	s_add_u32 s34, s34, s11
	s_addc_u32 s35, s35, 0
	s_add_u32 s14, s14, s38
	s_addc_u32 s15, s15, 0
	global_load_dwordx4 v[96:99], v3, s[34:35] sc0 sc1 nt
	s_add_u32 s34, s34, s32
	s_addc_u32 s35, s35, 0
	global_load_dwordx4 v[100:103], v3, s[34:35] sc0 sc1 nt
	s_add_u32 s34, s34, s32
	s_addc_u32 s35, s35, 0
	global_load_dwordx4 v[104:107], v3, s[34:35] sc0 sc1 nt
	s_add_u32 s34, s34, s32
	s_addc_u32 s35, s35, 0
	global_load_dwordx4 v[108:111], v3, s[34:35] sc0 sc1 nt
	s_add_u32 s34, s34, s32
	s_addc_u32 s35, s35, 0
	global_load_dwordx4 v[112:115], v3, s[34:35] sc0 sc1 nt
	s_add_u32 s34, s34, s32
	s_addc_u32 s35, s35, 0
	global_load_dwordx4 v[116:119], v3, s[34:35] sc0 sc1 nt
	s_add_u32 s34, s34, s32
	s_addc_u32 s35, s35, 0
	global_load_dwordx4 v[120:123], v3, s[34:35] sc0 sc1 nt
	s_add_u32 s34, s34, s32
	s_addc_u32 s35, s35, 0
	global_load_dwordx4 v[124:127], v3, s[34:35] sc0 sc1 nt
	s_add_u32 s34, s34, s32
	s_addc_u32 s35, s35, 0
	global_load_dwordx4 v[128:131], v3, s[34:35] sc0 sc1 nt
	s_add_u32 s34, s34, s32
	s_addc_u32 s35, s35, 0
	global_load_dwordx4 v[132:135], v3, s[34:35] sc0 sc1 nt
	s_add_u32 s34, s34, s32
	s_addc_u32 s35, s35, 0
	global_load_dwordx4 v[136:139], v3, s[34:35] sc0 sc1 nt
	s_add_u32 s34, s34, s32
	s_addc_u32 s35, s35, 0
	global_load_dwordx4 v[140:143], v3, s[34:35] sc0 sc1 nt
	s_add_u32 s34, s34, s32
	s_addc_u32 s35, s35, 0
	global_load_dwordx4 v[144:147], v3, s[34:35] sc0 sc1 nt
	s_add_u32 s34, s34, s32
	s_addc_u32 s35, s35, 0
	global_load_dwordx4 v[148:151], v3, s[34:35] sc0 sc1 nt
	s_add_u32 s34, s34, s32
	s_addc_u32 s35, s35, 0
	global_load_dwordx4 v[152:155], v3, s[34:35] sc0 sc1 nt
	s_add_u32 s34, s34, s32
	s_addc_u32 s35, s35, 0
	global_load_dwordx4 v[156:159], v3, s[34:35] sc0 sc1 nt
	s_waitcnt vmcnt(8)
	s_cmp_eq_u32 s10, 0
	s_cbranch_scc1 .Lbw_ng0
	v_readlane_b32 s36, v9, 0
	v_readlane_b32 s37, v9, 1
	v_readlane_b32 s38, v9, 2
	v_readlane_b32 s39, v9, 3
	s_nop 1
	v_mul_f32_e32 v96, s36, v96
	v_mul_f32_e32 v97, s36, v97
	v_mul_f32_e32 v98, s36, v98
	v_mul_f32_e32 v99, s36, v99
	v_mul_f32_e32 v100, s37, v100
	v_mul_f32_e32 v101, s37, v101
	v_mul_f32_e32 v102, s37, v102
	v_mul_f32_e32 v103, s37, v103
	v_mul_f32_e32 v104, s38, v104
	v_mul_f32_e32 v105, s38, v105
	v_mul_f32_e32 v106, s38, v106
	v_mul_f32_e32 v107, s38, v107
	v_mul_f32_e32 v108, s39, v108
	v_mul_f32_e32 v109, s39, v109
	v_mul_f32_e32 v110, s39, v110
	v_mul_f32_e32 v111, s39, v111
	v_readlane_b32 s36, v9, 4
	v_readlane_b32 s37, v9, 5
	v_readlane_b32 s38, v9, 6
	v_readlane_b32 s39, v9, 7
	s_nop 1
	v_mul_f32_e32 v112, s36, v112
	v_mul_f32_e32 v113, s36, v113
	v_mul_f32_e32 v114, s36, v114
	v_mul_f32_e32 v115, s36, v115
	v_mul_f32_e32 v116, s37, v116
	v_mul_f32_e32 v117, s37, v117
	v_mul_f32_e32 v118, s37, v118
	v_mul_f32_e32 v119, s37, v119
	v_mul_f32_e32 v120, s38, v120
	v_mul_f32_e32 v121, s38, v121
	v_mul_f32_e32 v122, s38, v122
	v_mul_f32_e32 v123, s38, v123
	v_mul_f32_e32 v124, s39, v124
	v_mul_f32_e32 v125, s39, v125
	v_mul_f32_e32 v126, s39, v126
	v_mul_f32_e32 v127, s39, v127
; #define LAS __attribute__((address_space(3)))
; #define GAS __attribute__((address_space(1)))
; #define SB() __builtin_amdgcn_sched_barrier(0)
; #define LDS_WAIT() asm volatile("s_waitcnt lgkmcnt(0)" ::: "memory")
; __device__ __forceinline__ unsigned cvt_pk_bf16(float lo, float hi) { unsigned r; asm volatile("v_cvt_pk_bf16_f32 %0, %1, %2" : "=v"(r) : "v"(lo), "v"(hi)); return r; }
; __device__ __forceinline__ void wg_convert_tile(Frame& F, const float* W, int ldw, bf16_t* WT, int Kd, int k0, int n0, int kind, const float* kgain) {
;     ...
;         for (int c = 0; c < 4; ++c) { const int n = 4 * lane + c;
;             u32x4 o; o.x = cvt_pk_bf16(ld[p & 1][0][c] * g[0], ld[p & 1][1][c] * g[1]); o.y = cvt_pk_bf16(ld[p & 1][2][c] * g[2], ld[p & 1][3][c] * g[3]);
;                      o.z = cvt_pk_bf16(ld[p & 1][4][c] * g[4], ld[p & 1][5][c] * g[5]); o.w = cvt_pk_bf16(ld[p & 1][6][c] * g[6], ld[p & 1][7][c] * g[7]);
;             *(LAS u32x4*)(img + n * 512 + ((kc ^ (unsigned)(lane & 31)) << 4)) = o; }
;         SB();
;     }
;     LDS_WAIT(); __syncthreads();
; #pragma unroll
;     for (int t = 0; t < 16; t += 4) { u32x4 v[4];
; #pragma unroll
;         for (int q = 0; q < 4; ++q) { const int idx = (t + q) * 512 + w * 64 + lane, n = idx >> 5, kc = idx & 31; v[q] = *(const LAS u32x4*)(img + n * 512 + ((kc ^ ((n >> 2) & 31)) << 4)); }
;         SB();
; #pragma unroll
;         for (int q = 0; q < 4; ++q) { const int idx = (t + q) * 512 + w * 64 + lane, n = idx >> 5, kc = idx & 31, nn = n0 + n;
;             const int row = kind < 0 ? nn : ((nn >> 7) * 256 + kind * 128 + (nn & 127));
;             __builtin_nontemporal_store(v[q], (GAS u32x4*)(WT + (size_t)row * Kd + k0 + 8 * kc)); }
;         SB(); }
;     LDS_WAIT(); __syncthreads();
.Lbw_ng0:
	v_cvt_pk_bf16_f32 v12, v96, v100
	v_cvt_pk_bf16_f32 v13, v104, v108
	v_cvt_pk_bf16_f32 v14, v112, v116
	v_cvt_pk_bf16_f32 v15, v120, v124
	v_xor_b32_e32 v11, 0, v6
	v_lshl_add_u32 v11, v11, 4, v5
	ds_write_b128 v11, v[12:15]
	v_cvt_pk_bf16_f32 v28, v97, v101
	v_cvt_pk_bf16_f32 v29, v105, v109
	v_cvt_pk_bf16_f32 v30, v113, v117
	v_cvt_pk_bf16_f32 v31, v121, v125
	v_xor_b32_e32 v16, 2, v6
	v_lshl_add_u32 v16, v16, 4, v5
	ds_write_b128 v16, v[28:31]
	v_cvt_pk_bf16_f32 v12, v98, v102
	v_cvt_pk_bf16_f32 v13, v106, v110
	v_cvt_pk_bf16_f32 v14, v114, v118
	v_cvt_pk_bf16_f32 v15, v122, v126
	v_xor_b32_e32 v11, 4, v6
	v_lshl_add_u32 v11, v11, 4, v5
	ds_write_b128 v11, v[12:15]
	v_cvt_pk_bf16_f32 v28, v99, v103
	v_cvt_pk_bf16_f32 v29, v107, v111
	v_cvt_pk_bf16_f32 v30, v115, v119
	v_cvt_pk_bf16_f32 v31, v123, v127
	v_xor_b32_e32 v16, 6, v6
	v_lshl_add_u32 v16, v16, 4, v5
	ds_write_b128 v16, v[28:31]
	s_waitcnt vmcnt(0)
	s_cmp_eq_u32 s10, 0
	s_cbranch_scc1 .Lbw_ng1
	v_readlane_b32 s36, v9, 8
	v_readlane_b32 s37, v9, 9
	v_readlane_b32 s38, v9, 10
	v_readlane_b32 s39, v9, 11
	s_nop 1
	v_mul_f32_e32 v128, s36, v128
	v_mul_f32_e32 v129, s36, v129
	v_mul_f32_e32 v130, s36, v130
	v_mul_f32_e32 v131, s36, v131
	v_mul_f32_e32 v132, s37, v132
	v_mul_f32_e32 v133, s37, v133
	v_mul_f32_e32 v134, s37, v134
	v_mul_f32_e32 v135, s37, v135
	v_mul_f32_e32 v136, s38, v136
	v_mul_f32_e32 v137, s38, v137
	v_mul_f32_e32 v138, s38, v138
	v_mul_f32_e32 v139, s38, v139
	v_mul_f32_e32 v140, s39, v140
	v_mul_f32_e32 v141, s39, v141
	v_mul_f32_e32 v142, s39, v142
	v_mul_f32_e32 v143, s39, v143
	v_readlane_b32 s36, v9, 12
	v_readlane_b32 s37, v9, 13
	v_readlane_b32 s38, v9, 14
	v_readlane_b32 s39, v9, 15
	s_nop 1
	v_mul_f32_e32 v144, s36, v144
	v_mul_f32_e32 v145, s36, v145
	v_mul_f32_e32 v146, s36, v146
	v_mul_f32_e32 v147, s36, v147
	v_mul_f32_e32 v148, s37, v148
	v_mul_f32_e32 v149, s37, v149
	v_mul_f32_e32 v150, s37, v150
	v_mul_f32_e32 v151, s37, v151
	v_mul_f32_e32 v152, s38, v152
	v_mul_f32_e32 v153, s38, v153
	v_mul_f32_e32 v154, s38, v154
	v_mul_f32_e32 v155, s38, v155
	v_mul_f32_e32 v156, s39, v156
	v_mul_f32_e32 v157, s39, v157
	v_mul_f32_e32 v158, s39, v158
	v_mul_f32_e32 v159, s39, v159
.Lbw_ng1:
	v_cvt_pk_bf16_f32 v12, v128, v132
	v_cvt_pk_bf16_f32 v13, v136, v140
	v_cvt_pk_bf16_f32 v14, v144, v148
	v_cvt_pk_bf16_f32 v15, v152, v156
	v_xor_b32_e32 v11, 1, v6
	v_lshl_add_u32 v11, v11, 4, v5
	ds_write_b128 v11, v[12:15]
	v_cvt_pk_bf16_f32 v28, v129, v133
	v_cvt_pk_bf16_f32 v29, v137, v141
	v_cvt_pk_bf16_f32 v30, v145, v149
	v_cvt_pk_bf16_f32 v31, v153, v157
	v_xor_b32_e32 v16, 3, v6
	v_lshl_add_u32 v16, v16, 4, v5
	ds_write_b128 v16, v[28:31]
	v_cvt_pk_bf16_f32 v12, v130, v134
	v_cvt_pk_bf16_f32 v13, v138, v142
	v_cvt_pk_bf16_f32 v14, v146, v150
	v_cvt_pk_bf16_f32 v15, v154, v158
	v_xor_b32_e32 v11, 5, v6
	v_lshl_add_u32 v11, v11, 4, v5
	ds_write_b128 v11, v[12:15]
	v_cvt_pk_bf16_f32 v28, v131, v135
	v_cvt_pk_bf16_f32 v29, v139, v143
	v_cvt_pk_bf16_f32 v30, v147, v151
	v_cvt_pk_bf16_f32 v31, v155, v159
	v_xor_b32_e32 v16, 7, v6
	v_lshl_add_u32 v16, v16, 4, v5
	ds_write_b128 v16, v[28:31]
	s_waitcnt lgkmcnt(0)
	ds_read_b128 v[96:99], v17
	ds_read_b128 v[100:103], v17 offset:1024
	ds_read_b128 v[104:107], v17 offset:2048
	ds_read_b128 v[108:111], v17 offset:3072
	s_waitcnt lgkmcnt(0)
	s_movk_i32 s36, 0
	s_mul_i32 s36, s36, s33
	s_add_u32 s38, s14, s36
	s_addc_u32 s39, s15, 0
	global_store_dwordx4 v8, v[96:99], s[38:39]
	s_movk_i32 s36, 32
	s_mul_i32 s36, s36, s33
	s_add_u32 s38, s14, s36
	s_addc_u32 s39, s15, 0
	global_store_dwordx4 v8, v[100:103], s[38:39]
	s_movk_i32 s36, 64
	s_mul_i32 s36, s36, s33
	s_add_u32 s38, s14, s36
	s_addc_u32 s39, s15, 0
	global_store_dwordx4 v8, v[104:107], s[38:39]
	s_movk_i32 s36, 96
	s_mul_i32 s36, s36, s33
	s_add_u32 s38, s14, s36
	s_addc_u32 s39, s15, 0
	global_store_dwordx4 v8, v[108:111], s[38:39]
	ds_read_b128 v[96:99], v17 offset:4096
	ds_read_b128 v[100:103], v17 offset:5120
	ds_read_b128 v[104:107], v17 offset:6144
	ds_read_b128 v[108:111], v17 offset:7168
	s_waitcnt lgkmcnt(0)
	s_movk_i32 s36, 128
	s_cmp_eq_u32 s10, 1
	s_cselect_b32 s36, 256, s36
	s_mul_i32 s36, s36, s33
	s_add_u32 s38, s14, s36
	s_addc_u32 s39, s15, 0
	global_store_dwordx4 v8, v[96:99], s[38:39]
	s_movk_i32 s36, 160
	s_cmp_eq_u32 s10, 1
	s_cselect_b32 s36, 288, s36
	s_mul_i32 s36, s36, s33
	s_add_u32 s38, s14, s36
	s_addc_u32 s39, s15, 0
	global_store_dwordx4 v8, v[100:103], s[38:39]
	s_movk_i32 s36, 192
	s_cmp_eq_u32 s10, 1
	s_cselect_b32 s36, 320, s36
	s_mul_i32 s36, s36, s33
	s_add_u32 s38, s14, s36
	s_addc_u32 s39, s15, 0
	global_store_dwordx4 v8, v[104:107], s[38:39]
	s_movk_i32 s36, 224
	s_cmp_eq_u32 s10, 1
	s_cselect_b32 s36, 352, s36
	s_mul_i32 s36, s36, s33
	s_add_u32 s38, s14, s36
	s_addc_u32 s39, s15, 0
	global_store_dwordx4 v8, v[108:111], s[38:39]
	s_mov_b64 exec, 0
